# speedup vs baseline: 1.0072x; 1.0054x over previous
_Z12fused_kernelPKtS0_PKfS0_S2_S2_Pf:
	s_load_dwordx4 s[4:7], s[0:1], 0x0
	s_load_dwordx2 s[44:45], s[0:1], 0x10
	s_load_dwordx2 s[46:47], s[0:1], 0x20
	s_movk_i32 s8, 0x120
	v_readfirstlane_b32 s3, v0
	v_cmp_gt_u32_e32 vcc, s8, v0
	v_mov_b32_e32 v3, 0
	v_mov_b32_e32 v4, 0
	s_getpc_b64 s[10:11]
	s_and_saveexec_b64 s[8:9], vcc
	s_cbranch_execz .LBB1_2
	v_lshlrev_b32_e32 v4, 6, v0
	v_mov_b32_e32 v5, 0
	v_lshl_add_u64 v[4:5], s[10:11], 0, v[4:5]
	global_load_dword v4, v[4:5], off
.LBB1_2:
	s_or_b64 exec, exec, s[8:9]
	s_ashr_i32 s9, s2, 3
	s_and_b32 s8, s2, 7
	s_and_b32 s9, s9, -8
	s_bfe_u32 s20, s3, 0x20006
	s_or_b32 s10, s9, s8
	s_lshl_b32 s2, s2, 4
	s_lshr_b32 s22, s3, 6
	v_bfe_u32 v1, v0, 5, 1
	s_and_b32 s2, s2, 0x380
	s_lshl_b32 s8, s20, 5
	s_ashr_i32 s11, s10, 31
	s_or_b32 s2, s8, s2
	s_lshl_b64 s[8:9], s[10:11], 19
	v_lshl_or_b32 v2, s22, 1, v1
	s_waitcnt lgkmcnt(0)
	s_cmpk_gt_u32 s3, 0xff
	s_cselect_b32 s44, s46, s44
	s_cselect_b32 s45, s47, s45
	v_and_b32_e32 v108, 0xff, v0
	v_lshlrev_b32_e32 v108, 2, v108
	global_load_dword v108, v108, s[44:45]
	s_add_u32 s14, s4, s8
	v_lshlrev_b32_e32 v6, 9, v2
	v_lshlrev_b32_e32 v2, 2, v2
	v_and_b32_e32 v5, 31, v0
	s_addc_u32 s15, s5, s9
	v_and_b32_e32 v2, 12, v2
	s_bfe_u32 s4, s3, 0x20007
	v_bitop3_b32 v2, v2, v5, s4 bitop3:0x36
	s_lshl_b32 s4, s22, 10
	v_lshl_or_b32 v192, v2, 4, v6
	s_add_i32 s21, s4, 0
	s_mov_b32 s4, m0
	s_mov_b32 m0, s21
	s_nop 0
	global_load_lds_dwordx4 v192, s[6:7]
	s_mov_b32 m0, s4
	s_add_u32 s4, s6, 0x2000
	s_addc_u32 s5, s7, 0
	s_add_i32 s31, s21, 0x2000
	s_mov_b32 s8, m0
	s_mov_b32 m0, s31
	s_nop 0
	global_load_lds_dwordx4 v192, s[4:5]
	s_mov_b32 m0, s8
	s_add_u32 s4, s6, 0x4000
	s_addc_u32 s5, s7, 0
	s_add_i32 s33, s21, 0x4000
	s_mov_b32 s8, m0
	s_mov_b32 m0, s33
	s_nop 0
	global_load_lds_dwordx4 v192, s[4:5]
	s_mov_b32 m0, s8
	s_add_u32 s4, s6, 0x6000
	s_addc_u32 s5, s7, 0
	s_add_i32 s34, s21, 0x6000
	s_mov_b32 s8, m0
	s_mov_b32 m0, s34
	s_nop 0
	global_load_lds_dwordx4 v192, s[4:5]
	s_mov_b32 m0, s8
	s_add_u32 s4, s6, 0x8000
	s_addc_u32 s5, s7, 0
	s_add_i32 s23, s21, 0x8000
	s_mov_b32 s8, m0
	s_mov_b32 m0, s23
	s_nop 0
	global_load_lds_dwordx4 v192, s[4:5]
	s_mov_b32 m0, s8
	s_add_u32 s4, s6, 0xa000
	s_addc_u32 s5, s7, 0
	s_add_i32 s24, s21, 0xa000
	s_mov_b32 s8, m0
	s_mov_b32 m0, s24
	s_nop 0
	global_load_lds_dwordx4 v192, s[4:5]
	s_mov_b32 m0, s8
	s_add_u32 s4, s6, 0xc000
	s_addc_u32 s5, s7, 0
	s_add_i32 s25, s21, 0xc000
	s_mov_b32 s8, m0
	s_mov_b32 m0, s25
	s_nop 0
	global_load_lds_dwordx4 v192, s[4:5]
	s_mov_b32 m0, s8
	s_add_u32 s4, s6, 0xe000
	s_addc_u32 s5, s7, 0
	s_add_i32 s26, s21, 0xe000
	s_mov_b32 s8, m0
	s_mov_b32 m0, s26
	s_nop 0
	global_load_lds_dwordx4 v192, s[4:5]
	s_mov_b32 m0, s8
	s_and_b32 s4, s2, 0x380
	s_lshl_b32 s4, s4, 9
	s_add_u32 s4, s14, s4
	s_addc_u32 s5, s15, 0
	s_add_i32 s27, s21, 0x10000
	s_add_i32 s28, s21, 0x12000
	s_add_i32 s29, s21, 0x14000
	s_add_i32 s30, s21, 0x16000
	s_mov_b32 s8, m0
	s_mov_b32 m0, s27
	s_nop 0
	global_load_lds_dwordx4 v192, s[4:5]
	s_mov_b32 m0, s8
	s_add_u32 s40, s4, 0x2000
	s_addc_u32 s41, s5, 0
	s_mov_b32 s8, m0
	s_mov_b32 m0, s28
	s_nop 0
	global_load_lds_dwordx4 v192, s[40:41]
	s_mov_b32 m0, s8
	s_add_u32 s40, s4, 0x4000
	s_addc_u32 s41, s5, 0
	s_mov_b32 s8, m0
	s_mov_b32 m0, s29
	s_nop 0
	global_load_lds_dwordx4 v192, s[40:41]
	s_mov_b32 m0, s8
	s_add_u32 s40, s4, 0x6000
	s_addc_u32 s41, s5, 0
	s_mov_b32 s8, m0
	s_mov_b32 m0, s30
	s_nop 0
	global_load_lds_dwordx4 v192, s[40:41]
	s_mov_b32 m0, s8
	s_add_u32 s40, s4, 0x8000
	s_addc_u32 s41, s5, 0
	s_add_i32 s42, s21, 0x18000
	s_mov_b32 s8, m0
	s_mov_b32 m0, s42
	s_nop 0
	global_load_lds_dwordx4 v192, s[40:41]
	s_mov_b32 m0, s8
	s_add_u32 s40, s4, 0xa000
	s_addc_u32 s41, s5, 0
	s_add_i32 s42, s21, 0x1a000
	s_mov_b32 s8, m0
	s_mov_b32 m0, s42
	s_nop 0
	global_load_lds_dwordx4 v192, s[40:41]
	s_mov_b32 m0, s8
	s_add_u32 s40, s4, 0xc000
	s_addc_u32 s41, s5, 0
	s_add_i32 s42, s21, 0x1c000
	s_mov_b32 s8, m0
	s_mov_b32 m0, s42
	s_nop 0
	global_load_lds_dwordx4 v192, s[40:41]
	s_mov_b32 m0, s8
	s_add_u32 s40, s4, 0xe000
	s_addc_u32 s41, s5, 0
	s_add_i32 s42, s21, 0x1e000
	s_mov_b32 s8, m0
	s_mov_b32 m0, s42
	s_nop 0
	global_load_lds_dwordx4 v192, s[40:41]
	s_mov_b32 m0, s8
	s_load_dwordx2 s[8:9], s[0:1], 0x18
	s_load_dwordx2 s[12:13], s[0:1], 0x28
	v_and_b32_e32 v81, 63, v0
	v_lshlrev_b32_e32 v2, 2, v0
	v_add_u32_e32 v6, 0x22000, v2
	s_waitcnt vmcnt(16)
	ds_write_b32 v6, v108
	s_lshr_b32 s5, s3, 8
	s_lshl_b32 s16, s20, 12
	s_lshl_b32 s4, s5, 5
	s_add_i32 s35, s16, 0
	s_add_u32 s18, s6, 0x18000
	v_and_b32_e32 v2, 12, v2
	v_bfe_u32 v0, v0, 2, 2
	s_addc_u32 s19, s7, 0
	v_bitop3_b32 v0, v2, v1, v0 bitop3:0x36
	s_add_u32 s16, s14, 0x8000
	v_lshlrev_b32_e32 v100, 4, v0
	v_or_b32_e32 v0, s4, v5
	s_addc_u32 s17, s15, 0
	s_lshl_b32 s36, s5, 7
	v_lshl_add_u32 v101, v0, 9, 0
	v_lshl_or_b32 v0, v1, 4, s36
	v_add_u32_e32 v0, 0, v0
	v_add_u32_e32 v83, v101, v100
	s_waitcnt vmcnt(0)
	s_waitcnt lgkmcnt(0)
	s_barrier
	s_lshl_b32 s40, s20, 14
	s_add_i32 s40, s40, 0x10000
	v_lshl_add_u32 v108, v5, 9, s40
	v_add_u32_e32 v109, v108, v100
	ds_read_b128 v[68:71], v109
	ds_read_b128 v[76:79], v109 offset:256
	v_xor_b32_e32 v109, 0x20, v100
	v_add_u32_e32 v109, v108, v109
	ds_read_b128 v[60:63], v109
	ds_read_b128 v[72:75], v109 offset:256
	v_xor_b32_e32 v109, 0x40, v100
	v_add_u32_e32 v109, v108, v109
	ds_read_b128 v[52:55], v109
	ds_read_b128 v[64:67], v109 offset:256
	v_xor_b32_e32 v109, 0x60, v100
	v_add_u32_e32 v109, v108, v109
	ds_read_b128 v[48:51], v109
	ds_read_b128 v[56:59], v109 offset:256
	v_xor_b32_e32 v109, 0x80, v100
	v_add_u32_e32 v109, v108, v109
	ds_read_b128 v[36:39], v109
	ds_read_b128 v[44:47], v109 offset:256
	v_xor_b32_e32 v109, 0xa0, v100
	v_add_u32_e32 v109, v108, v109
	ds_read_b128 v[28:31], v109
	ds_read_b128 v[40:43], v109 offset:256
	v_xor_b32_e32 v109, 0xc0, v100
	v_add_u32_e32 v109, v108, v109
	ds_read_b128 v[24:27], v109
	ds_read_b128 v[32:35], v109 offset:256
	v_xor_b32_e32 v109, 0xe0, v100
	v_add_u32_e32 v109, v108, v109
	ds_read_b128 v[20:23], v109
	ds_read_b128 v[16:19], v109 offset:256
	s_waitcnt lgkmcnt(0)
	s_barrier
	s_add_u32 s40, s6, 0x10000
	s_addc_u32 s41, s7, 0
	s_mov_b32 s42, m0
	s_mov_b32 m0, s27
	s_nop 0
	global_load_lds_dwordx4 v192, s[40:41]
	s_mov_b32 m0, s42
	s_add_u32 s40, s6, 0x12000
	s_addc_u32 s41, s7, 0
	s_mov_b32 s42, m0
	s_mov_b32 m0, s28
	s_nop 0
	global_load_lds_dwordx4 v192, s[40:41]
	s_mov_b32 m0, s42
	s_add_u32 s40, s6, 0x14000
	s_addc_u32 s41, s7, 0
	s_mov_b32 s42, m0
	s_mov_b32 m0, s29
	s_nop 0
	global_load_lds_dwordx4 v192, s[40:41]
	s_mov_b32 m0, s42
	s_add_u32 s40, s6, 0x16000
	s_addc_u32 s41, s7, 0
	s_mov_b32 s42, m0
	s_mov_b32 m0, s30
	s_nop 0
	global_load_lds_dwordx4 v192, s[40:41]
	s_mov_b32 m0, s42
	v_add_u32_e32 v80, 0x22000, v0
	ds_read_b128 v[84:87], v83
	ds_read_b128 v[0:3], v80
	ds_read_b128 v[4:7], v80 offset:32
	ds_read_b128 v[8:11], v80 offset:64
	ds_read_b128 v[12:15], v80 offset:96
	ds_read_b128 v[88:91], v83 offset:256
	s_waitcnt vmcnt(15) lgkmcnt(1)
	v_mfma_f32_32x32x16_bf16 v[0:15], v[84:87], v[68:71], v[0:15]
	v_xor_b32_e32 v102, 32, v100
	v_add_u32_e32 v84, v101, v102
	v_xor_b32_e32 v103, 64, v100
	v_add_u32_e32 v85, v101, v103
	v_xor_b32_e32 v104, 0x60, v100
	v_xor_b32_e32 v105, 0x80, v100
	v_xor_b32_e32 v106, 0xa0, v100
	s_waitcnt vmcnt(7) lgkmcnt(0)
	v_mfma_f32_32x32x16_bf16 v[0:15], v[88:91], v[76:79], v[0:15]
	ds_read_b128 v[86:89], v84
	ds_read_b128 v[90:93], v84 offset:256
	v_xor_b32_e32 v107, 0xe0, v100
	v_lshl_add_u32 v81, v81, 4, s35
	v_add_u32_e32 v81, 0x18000, v81
	v_lshl_add_u32 v82, s5, 11, v81
	s_add_u32 s36, s6, 0x1a000
	s_addc_u32 s37, s7, 0
	s_waitcnt lgkmcnt(1)
	v_mfma_f32_32x32x16_bf16 v[0:15], v[86:89], v[60:63], v[0:15]
	s_add_u32 s38, s6, 0x1c000
	s_addc_u32 s39, s7, 0
	s_add_u32 s6, s6, 0x1e000
	s_addc_u32 s7, s7, 0
	s_waitcnt vmcnt(6) lgkmcnt(0)
	v_mfma_f32_32x32x16_bf16 v[0:15], v[90:93], v[72:75], v[0:15]
	ds_read_b128 v[86:89], v85
	ds_read_b128 v[90:93], v85 offset:256
	s_waitcnt lgkmcnt(1)
	v_mfma_f32_32x32x16_bf16 v[0:15], v[86:89], v[52:55], v[0:15]
	v_add_u32_e32 v86, v101, v104
	v_add_u32_e32 v87, v101, v105
	s_waitcnt vmcnt(5) lgkmcnt(0)
	v_mfma_f32_32x32x16_bf16 v[0:15], v[90:93], v[64:67], v[0:15]
	ds_read_b128 v[88:91], v86
	ds_read_b128 v[92:95], v86 offset:256
	s_waitcnt lgkmcnt(1)
	v_mfma_f32_32x32x16_bf16 v[0:15], v[88:91], v[48:51], v[0:15]
	s_waitcnt vmcnt(4) lgkmcnt(0)
	v_mfma_f32_32x32x16_bf16 v[0:15], v[92:95], v[56:59], v[0:15]
	ds_read_b128 v[88:91], v87
	ds_read_b128 v[92:95], v87 offset:256
	s_waitcnt lgkmcnt(1)
	v_mfma_f32_32x32x16_bf16 v[0:15], v[88:91], v[36:39], v[0:15]
	v_add_u32_e32 v88, v101, v106
	v_add_u32_e32 v89, v101, v107
	s_waitcnt vmcnt(3) lgkmcnt(0)
	v_mfma_f32_32x32x16_bf16 v[0:15], v[92:95], v[44:47], v[0:15]
	ds_read_b128 v[90:93], v88
	ds_read_b128 v[94:97], v88 offset:256
	s_waitcnt lgkmcnt(1)
	v_mfma_f32_32x32x16_bf16 v[0:15], v[90:93], v[28:31], v[0:15]
	v_xor_b32_e32 v91, 0xc0, v100
	v_add_u32_e32 v90, v101, v91
	v_add_u32_e32 v101, 0x10000, v101
	v_add_u32_e32 v100, v101, v100
	v_add_u32_e32 v91, v101, v91
	s_waitcnt vmcnt(2) lgkmcnt(0)
	v_mfma_f32_32x32x16_bf16 v[0:15], v[94:97], v[40:43], v[0:15]
	ds_read_b128 v[92:95], v90
	ds_read_b128 v[96:99], v90 offset:256
	s_waitcnt lgkmcnt(1)
	v_mfma_f32_32x32x16_bf16 v[0:15], v[92:95], v[24:27], v[0:15]
	ds_read_b128 v[92:95], v89
	s_waitcnt vmcnt(1) lgkmcnt(1)
	v_mfma_f32_32x32x16_bf16 v[0:15], v[96:99], v[32:35], v[0:15]
	ds_read_b128 v[96:99], v89 offset:256
	s_waitcnt lgkmcnt(1)
	v_mfma_f32_32x32x16_bf16 v[0:15], v[92:95], v[20:23], v[0:15]
	s_waitcnt vmcnt(0) lgkmcnt(0)
	v_mfma_f32_32x32x16_bf16 v[0:15], v[96:99], v[16:19], v[0:15]
	s_nop 11
	v_cvt_pk_bf16_f32 v0, v0, v1
	v_cvt_pk_bf16_f32 v1, v2, v3
	v_cvt_pk_bf16_f32 v2, v4, v5
	v_cvt_pk_bf16_f32 v3, v6, v7
	v_cvt_pk_bf16_f32 v4, v8, v9
	v_cvt_pk_bf16_f32 v5, v10, v11
	v_cvt_pk_bf16_f32 v6, v12, v13
	v_cvt_pk_bf16_f32 v7, v14, v15
	ds_write_b128 v82, v[0:3]
	ds_write_b128 v82, v[4:7] offset:1024
	s_waitcnt lgkmcnt(0)
	s_barrier
	s_mov_b32 s5, m0
	s_mov_b32 m0, s21
	s_nop 0
	global_load_lds_dwordx4 v192, s[18:19]
	s_mov_b32 m0, s5
	s_nop 0
	s_mov_b32 s5, m0
	s_mov_b32 m0, s31
	s_nop 0
	global_load_lds_dwordx4 v192, s[36:37]
	s_mov_b32 m0, s5
	s_nop 0
	s_mov_b32 s5, m0
	s_mov_b32 m0, s33
	s_nop 0
	global_load_lds_dwordx4 v192, s[38:39]
	s_mov_b32 m0, s5
	s_nop 0
	s_mov_b32 s5, m0
	s_mov_b32 m0, s34
	s_nop 0
	global_load_lds_dwordx4 v192, s[6:7]
	s_mov_b32 m0, s5
	ds_read_b128 v[0:3], v80 offset:256
	ds_read2_b32 v[4:5], v80 offset0:72 offset1:73
	ds_read_b128 v[92:95], v83 offset:32768
	ds_read2_b32 v[6:7], v80 offset0:74 offset1:75
	ds_read2_b32 v[8:9], v80 offset0:80 offset1:81
	ds_read2_b32 v[10:11], v80 offset0:82 offset1:83
	ds_read2_b32 v[12:13], v80 offset0:88 offset1:89
	ds_read2_b32 v[14:15], v80 offset0:90 offset1:91
	ds_read_b128 v[96:99], v83 offset:33024
	s_waitcnt lgkmcnt(1)
	v_mfma_f32_32x32x16_bf16 v[0:15], v[92:95], v[68:71], v[0:15]
	s_add_u32 s6, s14, 0x2000
	s_addc_u32 s7, s15, 0
	s_add_u32 s18, s14, 0x4000
	s_addc_u32 s19, s15, 0
	s_add_u32 s34, s14, 0x6000
	s_addc_u32 s35, s15, 0
	s_waitcnt lgkmcnt(0)
	v_mfma_f32_32x32x16_bf16 v[0:15], v[96:99], v[76:79], v[0:15]
	ds_read_b128 v[92:95], v84 offset:32768
	ds_read_b128 v[96:99], v84 offset:33024
	s_waitcnt lgkmcnt(1)
	v_mfma_f32_32x32x16_bf16 v[0:15], v[92:95], v[60:63], v[0:15]
	s_waitcnt lgkmcnt(0)
	v_mfma_f32_32x32x16_bf16 v[0:15], v[96:99], v[72:75], v[0:15]
	ds_read_b128 v[92:95], v85 offset:32768
	ds_read_b128 v[96:99], v85 offset:33024
	s_waitcnt lgkmcnt(1)
	v_mfma_f32_32x32x16_bf16 v[0:15], v[92:95], v[52:55], v[0:15]
	s_waitcnt lgkmcnt(0)
	v_mfma_f32_32x32x16_bf16 v[0:15], v[96:99], v[64:67], v[0:15]
	ds_read_b128 v[92:95], v86 offset:32768
	ds_read_b128 v[96:99], v86 offset:33024
	s_waitcnt lgkmcnt(1)
	v_mfma_f32_32x32x16_bf16 v[0:15], v[92:95], v[48:51], v[0:15]
	s_waitcnt lgkmcnt(0)
	v_mfma_f32_32x32x16_bf16 v[0:15], v[96:99], v[56:59], v[0:15]
	ds_read_b128 v[92:95], v87 offset:32768
	ds_read_b128 v[96:99], v87 offset:33024
	s_waitcnt lgkmcnt(1)
	v_mfma_f32_32x32x16_bf16 v[0:15], v[92:95], v[36:39], v[0:15]
	s_waitcnt lgkmcnt(0)
	v_mfma_f32_32x32x16_bf16 v[0:15], v[96:99], v[44:47], v[0:15]
	ds_read_b128 v[92:95], v88 offset:32768
	ds_read_b128 v[96:99], v88 offset:33024
	s_waitcnt lgkmcnt(1)
	v_mfma_f32_32x32x16_bf16 v[0:15], v[92:95], v[28:31], v[0:15]
	s_waitcnt lgkmcnt(0)
	v_mfma_f32_32x32x16_bf16 v[0:15], v[96:99], v[40:43], v[0:15]
	ds_read_b128 v[92:95], v90 offset:32768
	ds_read_b128 v[96:99], v90 offset:33024
	s_waitcnt lgkmcnt(1)
	v_mfma_f32_32x32x16_bf16 v[0:15], v[92:95], v[24:27], v[0:15]
	ds_read_b128 v[92:95], v89 offset:32768
	s_waitcnt lgkmcnt(1)
	v_mfma_f32_32x32x16_bf16 v[0:15], v[96:99], v[32:35], v[0:15]
	ds_read_b128 v[96:99], v89 offset:33024
	ds_read_b128 v[128:131], v81
	ds_read_b128 v[132:135], v81 offset:1024
	ds_read_b128 v[136:139], v81 offset:2048
	ds_read_b128 v[140:143], v81 offset:3072
	s_waitcnt lgkmcnt(5)
	v_mfma_f32_32x32x16_bf16 v[0:15], v[92:95], v[20:23], v[0:15]
	s_waitcnt lgkmcnt(4)
	v_mfma_f32_32x32x16_bf16 v[0:15], v[96:99], v[16:19], v[0:15]
	s_nop 11
	v_cvt_pk_bf16_f32 v0, v0, v1
	v_cvt_pk_bf16_f32 v1, v2, v3
	v_cvt_pk_bf16_f32 v2, v4, v5
	v_cvt_pk_bf16_f32 v3, v6, v7
	v_cvt_pk_bf16_f32 v4, v8, v9
	v_cvt_pk_bf16_f32 v5, v10, v11
	v_cvt_pk_bf16_f32 v6, v12, v13
	v_cvt_pk_bf16_f32 v7, v14, v15
	ds_write_b128 v82, v[0:3] offset:20480
	ds_write_b128 v82, v[4:7] offset:21504
	s_waitcnt vmcnt(4) lgkmcnt(0)
	s_barrier
	s_mov_b32 s5, m0
	s_mov_b32 m0, s23
	s_nop 0
	global_load_lds_dwordx4 v192, s[14:15]
	s_mov_b32 m0, s5
	s_nop 0
	s_mov_b32 s5, m0
	s_mov_b32 m0, s24
	s_nop 0
	global_load_lds_dwordx4 v192, s[6:7]
	s_mov_b32 m0, s5
	s_add_u32 s6, s14, 0xa000
	s_mov_b32 s5, m0
	s_mov_b32 m0, s25
	s_nop 0
	global_load_lds_dwordx4 v192, s[18:19]
	s_mov_b32 m0, s5
	s_addc_u32 s7, s15, 0
	s_mov_b32 s5, m0
	s_mov_b32 m0, s26
	s_nop 0
	global_load_lds_dwordx4 v192, s[34:35]
	s_mov_b32 m0, s5
	ds_read_b128 v[0:3], v80 offset:512
	ds_read2_b32 v[4:5], v80 offset0:136 offset1:137
	ds_read_b128 v[92:95], v100
	ds_read2_b32 v[6:7], v80 offset0:138 offset1:139
	ds_read2_b32 v[8:9], v80 offset0:144 offset1:145
	ds_read2_b32 v[10:11], v80 offset0:146 offset1:147
	ds_read2_b32 v[12:13], v80 offset0:152 offset1:153
	ds_read2_b32 v[14:15], v80 offset0:154 offset1:155
	ds_read_b128 v[96:99], v100 offset:256
	s_waitcnt lgkmcnt(1)
	v_mfma_f32_32x32x16_bf16 v[0:15], v[92:95], v[68:71], v[0:15]
	v_add_u32_e32 v100, v101, v102
	s_add_u32 s18, s14, 0xc000
	s_addc_u32 s19, s15, 0
	s_add_u32 s34, s14, 0xe000
	s_addc_u32 s35, s15, 0
	s_cmpk_gt_u32 s3, 0xff
	s_waitcnt lgkmcnt(0)
	v_mfma_f32_32x32x16_bf16 v[0:15], v[96:99], v[76:79], v[0:15]
	ds_read_b128 v[92:95], v100
	ds_read_b128 v[96:99], v100 offset:256
	v_add_u32_e32 v100, v101, v103
	s_waitcnt lgkmcnt(1)
	v_mfma_f32_32x32x16_bf16 v[0:15], v[92:95], v[60:63], v[0:15]
	s_waitcnt lgkmcnt(0)
	v_mfma_f32_32x32x16_bf16 v[0:15], v[96:99], v[72:75], v[0:15]
	ds_read_b128 v[92:95], v100
	ds_read_b128 v[96:99], v100 offset:256
	v_add_u32_e32 v100, v101, v104
	s_waitcnt lgkmcnt(1)
	v_mfma_f32_32x32x16_bf16 v[0:15], v[92:95], v[52:55], v[0:15]
	s_waitcnt lgkmcnt(0)
	v_mfma_f32_32x32x16_bf16 v[0:15], v[96:99], v[64:67], v[0:15]
	ds_read_b128 v[92:95], v100
	ds_read_b128 v[96:99], v100 offset:256
	v_add_u32_e32 v100, v101, v105
	s_waitcnt lgkmcnt(1)
	v_mfma_f32_32x32x16_bf16 v[0:15], v[92:95], v[48:51], v[0:15]
	s_waitcnt lgkmcnt(0)
	v_mfma_f32_32x32x16_bf16 v[0:15], v[96:99], v[56:59], v[0:15]
	ds_read_b128 v[92:95], v100
	ds_read_b128 v[96:99], v100 offset:256
	v_add_u32_e32 v100, v101, v106
	s_waitcnt lgkmcnt(1)
	v_mfma_f32_32x32x16_bf16 v[0:15], v[92:95], v[36:39], v[0:15]
	s_waitcnt lgkmcnt(0)
	v_mfma_f32_32x32x16_bf16 v[0:15], v[96:99], v[44:47], v[0:15]
	ds_read_b128 v[92:95], v100
	ds_read_b128 v[96:99], v100 offset:256
	s_waitcnt lgkmcnt(1)
	v_mfma_f32_32x32x16_bf16 v[0:15], v[92:95], v[28:31], v[0:15]
	s_waitcnt lgkmcnt(0)
	v_mfma_f32_32x32x16_bf16 v[0:15], v[96:99], v[40:43], v[0:15]
	ds_read_b128 v[92:95], v91
	ds_read_b128 v[96:99], v91 offset:256
	v_add_u32_e32 v91, v101, v107
	s_waitcnt lgkmcnt(1)
	v_mfma_f32_32x32x16_bf16 v[0:15], v[92:95], v[24:27], v[0:15]
	ds_read_b128 v[92:95], v91
	s_waitcnt lgkmcnt(1)
	v_mfma_f32_32x32x16_bf16 v[0:15], v[96:99], v[32:35], v[0:15]
	ds_read_b128 v[96:99], v91 offset:256
	ds_read_b128 v[144:147], v81 offset:20480
	ds_read_b128 v[148:151], v81 offset:21504
	ds_read_b128 v[152:155], v81 offset:22528
	ds_read_b128 v[156:159], v81 offset:23552
	s_waitcnt lgkmcnt(5)
	v_mfma_f32_32x32x16_bf16 v[0:15], v[92:95], v[20:23], v[0:15]
	s_waitcnt lgkmcnt(4)
	v_mfma_f32_32x32x16_bf16 v[0:15], v[96:99], v[16:19], v[0:15]
	s_nop 11
	v_cvt_pk_bf16_f32 v0, v0, v1
	v_cvt_pk_bf16_f32 v1, v2, v3
	v_cvt_pk_bf16_f32 v2, v4, v5
	v_cvt_pk_bf16_f32 v3, v6, v7
	v_cvt_pk_bf16_f32 v4, v8, v9
	v_cvt_pk_bf16_f32 v5, v10, v11
	v_cvt_pk_bf16_f32 v6, v12, v13
	v_cvt_pk_bf16_f32 v7, v14, v15
	ds_write_b128 v82, v[0:3]
	ds_write_b128 v82, v[4:7] offset:1024
	s_waitcnt vmcnt(4) lgkmcnt(0)
	s_barrier
	s_mov_b32 s5, m0
	s_mov_b32 m0, s27
	s_nop 0
	global_load_lds_dwordx4 v192, s[16:17]
	s_mov_b32 m0, s5
	s_nop 0
	s_mov_b32 s5, m0
	s_mov_b32 m0, s28
	s_nop 0
	global_load_lds_dwordx4 v192, s[6:7]
	s_mov_b32 m0, s5
	s_movk_i32 s7, 0x80
	s_mov_b32 s5, m0
	s_mov_b32 m0, s29
	s_nop 0
	global_load_lds_dwordx4 v192, s[18:19]
	s_mov_b32 m0, s5
	s_movk_i32 s6, 0xc0
	s_mov_b32 s5, m0
	s_mov_b32 m0, s30
	s_nop 0
	global_load_lds_dwordx4 v192, s[34:35]
	s_mov_b32 m0, s5
	ds_read_b128 v[0:3], v80 offset:768
	ds_read2_b32 v[4:5], v80 offset0:200 offset1:201
	ds_read_b128 v[92:95], v83
	ds_read2_b32 v[6:7], v80 offset0:202 offset1:203
	ds_read2_b32 v[8:9], v80 offset0:208 offset1:209
	ds_read2_b32 v[10:11], v80 offset0:210 offset1:211
	ds_read2_b32 v[12:13], v80 offset0:216 offset1:217
	ds_read2_b32 v[14:15], v80 offset0:218 offset1:219
	ds_read_b128 v[96:99], v83 offset:256
	s_waitcnt lgkmcnt(1)
	v_mfma_f32_32x32x16_bf16 v[0:15], v[92:95], v[68:71], v[0:15]
	s_mov_b32 s5, 0x10000
	s_waitcnt lgkmcnt(0)
	v_mfma_f32_32x32x16_bf16 v[0:15], v[96:99], v[76:79], v[0:15]
	ds_read_b128 v[68:71], v84
	ds_read_b128 v[76:79], v84 offset:256
	s_waitcnt lgkmcnt(1)
	v_mfma_f32_32x32x16_bf16 v[0:15], v[68:71], v[60:63], v[0:15]
	ds_read_b128 v[60:63], v85
	ds_read_b128 v[68:71], v85 offset:256
	s_waitcnt lgkmcnt(2)
	v_mfma_f32_32x32x16_bf16 v[0:15], v[76:79], v[72:75], v[0:15]
	s_waitcnt lgkmcnt(1)
	v_mfma_f32_32x32x16_bf16 v[0:15], v[60:63], v[52:55], v[0:15]
	ds_read_b128 v[52:55], v86
	ds_read_b128 v[60:63], v86 offset:256
	s_waitcnt lgkmcnt(2)
	v_mfma_f32_32x32x16_bf16 v[0:15], v[68:71], v[64:67], v[0:15]
	s_waitcnt lgkmcnt(1)
	v_mfma_f32_32x32x16_bf16 v[0:15], v[52:55], v[48:51], v[0:15]
	ds_read_b128 v[48:51], v87
	ds_read_b128 v[52:55], v87 offset:256
	s_waitcnt lgkmcnt(2)
	v_mfma_f32_32x32x16_bf16 v[0:15], v[60:63], v[56:59], v[0:15]
	s_waitcnt lgkmcnt(1)
	v_mfma_f32_32x32x16_bf16 v[0:15], v[48:51], v[36:39], v[0:15]
	s_waitcnt lgkmcnt(0)
	v_mfma_f32_32x32x16_bf16 v[0:15], v[52:55], v[44:47], v[0:15]
	ds_read_b128 v[36:39], v88
	ds_read_b128 v[44:47], v88 offset:256
	s_waitcnt lgkmcnt(1)
	v_mfma_f32_32x32x16_bf16 v[0:15], v[36:39], v[28:31], v[0:15]
	ds_read_b128 v[28:31], v90
	ds_read_b128 v[36:39], v90 offset:256
	s_waitcnt lgkmcnt(2)
	v_mfma_f32_32x32x16_bf16 v[0:15], v[44:47], v[40:43], v[0:15]
	s_waitcnt lgkmcnt(1)
	v_mfma_f32_32x32x16_bf16 v[0:15], v[28:31], v[24:27], v[0:15]
	ds_read_b128 v[24:27], v89
	ds_read_b128 v[28:31], v89 offset:256
	ds_read_b128 v[160:163], v81
	ds_read_b128 v[164:167], v81 offset:1024
	ds_read_b128 v[168:171], v81 offset:2048
	ds_read_b128 v[172:175], v81 offset:3072
	s_waitcnt lgkmcnt(6)
	v_mfma_f32_32x32x16_bf16 v[0:15], v[36:39], v[32:35], v[0:15]
	s_waitcnt lgkmcnt(5)
	v_mfma_f32_32x32x16_bf16 v[0:15], v[24:27], v[20:23], v[0:15]
	v_mbcnt_lo_u32_b32 v20, -1, 0
	v_mbcnt_hi_u32_b32 v193, -1, v20
	v_mov_b32_e32 v194, v193
	s_waitcnt lgkmcnt(4)
	v_mfma_f32_32x32x16_bf16 v[0:15], v[28:31], v[16:19], v[0:15]
	s_nop 11
	v_cvt_pk_bf16_f32 v0, v0, v1
	v_cvt_pk_bf16_f32 v1, v2, v3
	v_cvt_pk_bf16_f32 v2, v4, v5
	v_cvt_pk_bf16_f32 v3, v6, v7
	v_cvt_pk_bf16_f32 v4, v8, v9
	v_cvt_pk_bf16_f32 v5, v10, v11
	v_cvt_pk_bf16_f32 v6, v12, v13
	v_cvt_pk_bf16_f32 v7, v14, v15
	ds_write_b128 v82, v[0:3] offset:20480
	ds_write_b128 v82, v[4:7] offset:21504
	s_waitcnt vmcnt(4) lgkmcnt(0)
	s_barrier
	ds_read_b128 v[176:179], v81 offset:20480
	ds_read_b128 v[180:183], v81 offset:21504
	ds_read_b128 v[184:187], v81 offset:22528
	ds_read_b128 v[188:191], v81 offset:23552
	s_waitcnt lgkmcnt(0)
	s_barrier
	s_nop 0
	v_and_b32_e32 v196, 31, v194
	v_ashrrev_i32_e32 v197, 5, v194
	v_lshlrev_b32_e32 v195, 2, v194
	v_bfe_u32 v198, v194, 2, 2
	s_cbranch_scc0 .LBB1_16
	v_lshl_add_u32 v0, s20, 2, v197
	v_lshlrev_b32_e32 v3, 2, v197
	v_add_u32_e32 v1, 2, v0
	v_lshlrev_b32_e32 v2, 9, v0
	v_and_b32_e32 v3, 12, v3
	v_bfe_u32 v0, v0, 2, 2
	v_bitop3_b32 v0, v0, v196, v3 bitop3:0x36
	v_lshl_or_b32 v199, v0, 4, v2
	v_lshlrev_b32_e32 v0, 2, v1
	s_bfe_u32 s18, s3, 0x10006
	v_and_b32_e32 v0, 12, v0
	v_bfe_u32 v2, v1, 2, 2
	v_bitop3_b32 v0, v0, v196, v2 bitop3:0x36
	v_lshrrev_b32_e32 v2, 3, v194
	s_lshl_b32 s16, s18, 8
	v_and_b32_e32 v2, 2, v2
	v_bfe_u32 v3, v194, 1, 1
	s_add_i32 s16, s16, 0
	v_lshlrev_b32_e32 v4, 3, v194
	v_lshl_add_u32 v5, v197, 11, s16
	v_bitop3_b32 v2, v2, v197, v3 bitop3:0x36
	v_and_or_b32 v4, v4, 8, v5
	v_lshlrev_b32_e32 v2, 4, v2
	v_lshlrev_b32_e32 v3, 6, v198
	v_lshl_add_u32 v4, v198, 9, v4
	v_or_b32_e32 v5, v2, v3
	v_add_u32_e32 v200, v4, v5
	v_bitop3_b32 v5, v2, v3, 32 bitop3:0xde
	v_add_u32_e32 v6, 0x1000, v4
	v_add_u32_e32 v201, v6, v5
	v_xor_b32_e32 v5, 64, v3
	v_bitop3_b32 v5, v2, v5, 32 bitop3:0xde
	v_add_u32_e32 v203, v6, v5
	v_xor_b32_e32 v5, 0x80, v3
	v_bitop3_b32 v7, v2, v3, 64 bitop3:0xf6
	v_bitop3_b32 v5, v2, v5, 32 bitop3:0xde
	v_add_u32_e32 v202, v4, v7
	v_bitop3_b32 v7, v2, v3, s7 bitop3:0xf6
	v_add_u32_e32 v205, v6, v5
	v_xor_b32_e32 v5, 0xc0, v3
	v_bitop3_b32 v3, v2, v3, s6 bitop3:0xf6
	s_and_b32 s6, s22, 2
	v_lshlrev_b32_e32 v1, 9, v1
	s_lshl_b32 s27, s6, 2
	s_lshl_b32 s7, s6, 8
	s_lshl_b32 s6, s6, 12
	v_lshl_or_b32 v208, v0, 4, v1
	s_lshl_b32 s19, s20, 11
	s_add_i32 s7, s7, 0
	s_add_i32 s6, s6, 0
	v_mov_b32_e32 v0, 0
	v_bitop3_b32 v2, v2, v5, 32 bitop3:0xde
	s_waitcnt vmcnt(0)
	s_add_i32 s19, s19, 0
	s_add_i32 s16, s7, 0x20000
	s_add_i32 s7, s7, 0x20100
	v_lshlrev_b32_e32 v209, 4, v194
	s_add_i32 s6, s6, 0x18000
	v_mov_b32_e32 v14, v0
	v_mov_b32_e32 v15, v0
	v_add_u32_e32 v204, v4, v7
	v_add_u32_e32 v206, v4, v3
	v_add_u32_e32 v207, v6, v2
	v_add_u32_e32 v212, s6, v209
	s_add_u32 s6, s8, 0xfff90000
	v_mov_b32_e32 v1, v0
	v_mov_b32_e32 v2, v0
	v_mov_b32_e32 v3, v0
	v_mov_b32_e32 v4, v0
	v_mov_b32_e32 v5, v0
	v_mov_b32_e32 v6, v0
	v_mov_b32_e32 v7, v0
	v_mov_b32_e32 v8, v0
	v_mov_b32_e32 v9, v0
	v_mov_b32_e32 v10, v0
	v_mov_b32_e32 v11, v0
	v_mov_b32_e32 v12, v0
	v_mov_b32_e32 v13, v0
	v_mov_b64_e32 v[62:63], v[14:15]
	v_mov_b64_e32 v[94:95], v[14:15]
	v_mov_b64_e32 v[126:127], v[14:15]
	v_mov_b64_e32 v[30:31], v[14:15]
	v_mov_b64_e32 v[46:47], v[14:15]
	v_mov_b64_e32 v[78:79], v[14:15]
	v_mov_b64_e32 v[110:111], v[14:15]
	v_add_u32_e32 v210, s16, v195
	v_add_u32_e32 v211, s7, v195
	s_addc_u32 s7, s9, -1
	s_mov_b32 s33, 1
	s_mov_b32 s31, 0x8000
	s_mov_b32 s29, 0x10000
	v_mov_b64_e32 v[60:61], v[12:13]
	v_mov_b64_e32 v[58:59], v[10:11]
	v_mov_b64_e32 v[56:57], v[8:9]
	v_mov_b64_e32 v[54:55], v[6:7]
	v_mov_b64_e32 v[52:53], v[4:5]
	v_mov_b64_e32 v[50:51], v[2:3]
	v_mov_b64_e32 v[48:49], v[0:1]
	v_mov_b64_e32 v[92:93], v[12:13]
	v_mov_b64_e32 v[90:91], v[10:11]
	v_mov_b64_e32 v[88:89], v[8:9]
	v_mov_b64_e32 v[86:87], v[6:7]
	v_mov_b64_e32 v[84:85], v[4:5]
	v_mov_b64_e32 v[82:83], v[2:3]
	v_mov_b64_e32 v[80:81], v[0:1]
	v_mov_b64_e32 v[124:125], v[12:13]
	v_mov_b64_e32 v[122:123], v[10:11]
	v_mov_b64_e32 v[120:121], v[8:9]
	v_mov_b64_e32 v[118:119], v[6:7]
	v_mov_b64_e32 v[116:117], v[4:5]
	v_mov_b64_e32 v[114:115], v[2:3]
	v_mov_b64_e32 v[112:113], v[0:1]
	v_mov_b64_e32 v[28:29], v[12:13]
	v_mov_b64_e32 v[26:27], v[10:11]
	v_mov_b64_e32 v[24:25], v[8:9]
	v_mov_b64_e32 v[22:23], v[6:7]
	v_mov_b64_e32 v[20:21], v[4:5]
	v_mov_b64_e32 v[18:19], v[2:3]
	v_mov_b64_e32 v[16:17], v[0:1]
	v_mov_b64_e32 v[44:45], v[12:13]
	v_mov_b64_e32 v[42:43], v[10:11]
	v_mov_b64_e32 v[40:41], v[8:9]
	v_mov_b64_e32 v[38:39], v[6:7]
	v_mov_b64_e32 v[36:37], v[4:5]
	v_mov_b64_e32 v[34:35], v[2:3]
	v_mov_b64_e32 v[32:33], v[0:1]
	v_mov_b64_e32 v[76:77], v[12:13]
	v_mov_b64_e32 v[74:75], v[10:11]
	v_mov_b64_e32 v[72:73], v[8:9]
	v_mov_b64_e32 v[70:71], v[6:7]
	v_mov_b64_e32 v[68:69], v[4:5]
	v_mov_b64_e32 v[66:67], v[2:3]
	v_mov_b64_e32 v[64:65], v[0:1]
	v_mov_b64_e32 v[108:109], v[12:13]
	v_mov_b64_e32 v[106:107], v[10:11]
	v_mov_b64_e32 v[104:105], v[8:9]
	v_mov_b64_e32 v[102:103], v[6:7]
	v_mov_b64_e32 v[100:101], v[4:5]
	v_mov_b64_e32 v[98:99], v[2:3]
	v_mov_b64_e32 v[96:97], v[0:1]
	s_waitcnt lgkmcnt(0)
	s_barrier

.LBB1_21:
	s_setprio 1
	v_add_u32_e32 v16, s5, v80
	ds_read_b128 v[32:35], v16
	ds_read_b128 v[36:39], v16 offset:256
	ds_read_b128 v[92:95], v16 offset:16384
	ds_read_b128 v[100:103], v16 offset:16640
	v_add_u32_e32 v16, s5, v81
	ds_read_b128 v[40:43], v16
	ds_read_b128 v[44:47], v16 offset:256
	ds_read_b128 v[104:107], v16 offset:16384
	ds_read_b128 v[108:111], v16 offset:16640
	s_waitcnt lgkmcnt(4)
	v_add_u32_e32 v91, s5, v82
	v_mfma_f32_32x32x16_bf16 v[16:31], v[32:35], v[128:131], v[0:15]
	ds_read_b128 v[32:35], v91
	v_mfma_f32_32x32x16_bf16 v[16:31], v[36:39], v[160:163], v[16:31]
	ds_read_b128 v[36:39], v91 offset:256
	ds_read_b128 v[112:115], v91 offset:16384
	ds_read_b128 v[116:119], v91 offset:16640
	s_waitcnt lgkmcnt(4)
	v_add_u32_e32 v91, s5, v83
	v_mfma_f32_32x32x16_bf16 v[16:31], v[40:43], v[132:135], v[16:31]
	ds_read_b128 v[40:43], v91
	v_mfma_f32_32x32x16_bf16 v[16:31], v[44:47], v[164:167], v[16:31]
	ds_read_b128 v[44:47], v91 offset:256
	ds_read_b128 v[120:123], v91 offset:16384
	ds_read_b128 v[124:127], v91 offset:16640
	s_waitcnt lgkmcnt(4)
	v_add_u32_e32 v91, s5, v84
	v_mfma_f32_32x32x16_bf16 v[16:31], v[32:35], v[136:139], v[16:31]
	ds_read_b128 v[32:35], v91
	v_mfma_f32_32x32x16_bf16 v[16:31], v[36:39], v[168:171], v[16:31]
	ds_read_b128 v[36:39], v91 offset:256
	ds_read_b128 v[194:197], v91 offset:16384
	ds_read_b128 v[198:201], v91 offset:16640
	s_waitcnt lgkmcnt(4)
	v_add_u32_e32 v91, s5, v85
	v_mfma_f32_32x32x16_bf16 v[16:31], v[40:43], v[140:143], v[16:31]
	ds_read_b128 v[40:43], v91
	v_mfma_f32_32x32x16_bf16 v[16:31], v[44:47], v[172:175], v[16:31]
	ds_read_b128 v[44:47], v91 offset:256
	ds_read_b128 v[202:205], v91 offset:16384
	ds_read_b128 v[206:209], v91 offset:16640
	s_waitcnt lgkmcnt(4)
	v_add_u32_e32 v91, s5, v86
	v_mfma_f32_32x32x16_bf16 v[16:31], v[32:35], v[144:147], v[16:31]
	ds_read_b128 v[32:35], v91
	v_mfma_f32_32x32x16_bf16 v[16:31], v[36:39], v[176:179], v[16:31]
	ds_read_b128 v[36:39], v91 offset:256
	ds_read_b128 v[210:213], v91 offset:16384
	ds_read_b128 v[214:217], v91 offset:16640
	s_waitcnt lgkmcnt(4)
	v_add_u32_e32 v91, s5, v87
	v_mfma_f32_32x32x16_bf16 v[16:31], v[40:43], v[148:151], v[16:31]
	ds_read_b128 v[40:43], v91
	v_mfma_f32_32x32x16_bf16 v[16:31], v[44:47], v[180:183], v[16:31]
	ds_read_b128 v[44:47], v91 offset:256
	ds_read_b128 v[218:221], v91 offset:16384
	ds_read_b128 v[222:225], v91 offset:16640
	s_waitcnt lgkmcnt(4)
	s_nop 0
	s_waitcnt lgkmcnt(0)
	v_mfma_f32_32x32x16_bf16 v[16:31], v[32:35], v[152:155], v[16:31]
	v_mfma_f32_32x32x16_bf16 v[16:31], v[36:39], v[184:187], v[16:31]
	v_mfma_f32_32x32x16_bf16 v[16:31], v[40:43], v[156:159], v[16:31]
	v_mfma_f32_32x32x16_bf16 v[16:31], v[44:47], v[188:191], v[16:31]
	s_setprio 0
	v_mfma_f32_32x32x16_bf16 v[32:47], v[92:95], v[128:131], v[0:15]
	s_and_b32 s13, s11, 1
	s_nop 8
	v_max_f32_e32 v91, v17, v17
	v_max_f32_e32 v92, v16, v16
	v_max_f32_e32 v91, v92, v91
	v_max3_f32 v91, v91, v18, v19
	v_max3_f32 v91, v91, v20, v21
	v_max3_f32 v91, v91, v22, v23
	v_max3_f32 v91, v91, v24, v25
	v_max3_f32 v91, v91, v26, v27
	v_mfma_f32_32x32x16_bf16 v[32:47], v[100:103], v[160:163], v[32:47]
	v_max3_f32 v91, v91, v28, v29
	v_max3_f32 v91, v91, v30, v31
	v_mfma_f32_32x32x16_bf16 v[32:47], v[104:107], v[132:135], v[32:47]
	v_mfma_f32_32x32x16_bf16 v[32:47], v[108:111], v[164:167], v[32:47]
	v_mfma_f32_32x32x16_bf16 v[32:47], v[112:115], v[136:139], v[32:47]
	v_mfma_f32_32x32x16_bf16 v[32:47], v[116:119], v[168:171], v[32:47]
	v_mfma_f32_32x32x16_bf16 v[32:47], v[120:123], v[140:143], v[32:47]
	v_mfma_f32_32x32x16_bf16 v[32:47], v[124:127], v[172:175], v[32:47]
	v_mfma_f32_32x32x16_bf16 v[32:47], v[194:197], v[144:147], v[32:47]
	v_mfma_f32_32x32x16_bf16 v[32:47], v[198:201], v[176:179], v[32:47]
	v_mfma_f32_32x32x16_bf16 v[32:47], v[202:205], v[148:151], v[32:47]
	v_mfma_f32_32x32x16_bf16 v[32:47], v[206:209], v[180:183], v[32:47]
	v_mfma_f32_32x32x16_bf16 v[32:47], v[210:213], v[152:155], v[32:47]
	v_mfma_f32_32x32x16_bf16 v[32:47], v[214:217], v[184:187], v[32:47]
	v_mfma_f32_32x32x16_bf16 v[32:47], v[218:221], v[156:159], v[32:47]
	v_mfma_f32_32x32x16_bf16 v[32:47], v[222:225], v[188:191], v[32:47]
	s_nop 11
	v_max3_f32 v91, v91, v32, v33
	v_max3_f32 v91, v91, v34, v35
	v_max3_f32 v91, v91, v36, v37
	v_max3_f32 v91, v91, v38, v39
	v_max3_f32 v91, v91, v40, v41
	v_max3_f32 v91, v91, v42, v43
	v_max3_f32 v91, v91, v44, v45
	v_max3_f32 v91, v91, v46, v47
	v_mov_b32_e32 v92, v91
	s_nop 1
	v_permlane32_swap_b32_e32 v91, v92
	v_max_f32_e32 v92, v92, v92
	v_max_f32_e32 v91, v91, v91
	v_max_f32_e32 v91, v91, v92
	v_cmp_ge_f32_e32 vcc, s12, v91
	s_cmp_eq_u64 vcc, exec
	s_cbranch_scc0 .LBB1_19
	s_mov_b32 s14, 0
	s_branch .LBB1_20

	.amdhsa_kernel _Z12fused_kernelPKtS0_PKfS0_S2_S2_Pf
		.amdhsa_group_segment_fixed_size 0
		.amdhsa_private_segment_fixed_size 0
		.amdhsa_kernarg_size 56
		.amdhsa_user_sgpr_count 2
		.amdhsa_user_sgpr_dispatch_ptr 0
		.amdhsa_user_sgpr_queue_ptr 0
		.amdhsa_user_sgpr_kernarg_segment_ptr 1
		.amdhsa_user_sgpr_dispatch_id 0
		.amdhsa_user_sgpr_kernarg_preload_length 0
		.amdhsa_user_sgpr_kernarg_preload_offset 0
		.amdhsa_user_sgpr_private_segment_size 0
		.amdhsa_uses_dynamic_stack 0
		.amdhsa_enable_private_segment 0
		.amdhsa_system_sgpr_workgroup_id_x 1
		.amdhsa_system_sgpr_workgroup_id_y 0
		.amdhsa_system_sgpr_workgroup_id_z 0
		.amdhsa_system_sgpr_workgroup_info 0
		.amdhsa_system_vgpr_workitem_id 0
		.amdhsa_next_free_vgpr 246
		.amdhsa_next_free_sgpr 48
		.amdhsa_accum_offset 248
		.amdhsa_reserve_vcc 1
		.amdhsa_float_round_mode_32 0
		.amdhsa_float_round_mode_16_64 0
		.amdhsa_float_denorm_mode_32 3
		.amdhsa_float_denorm_mode_16_64 3
		.amdhsa_dx10_clamp 1
		.amdhsa_ieee_mode 1
		.amdhsa_fp16_overflow 0
		.amdhsa_tg_split 0
		.amdhsa_exception_fp_ieee_invalid_op 0
		.amdhsa_exception_fp_denorm_src 0
		.amdhsa_exception_fp_ieee_div_zero 0
		.amdhsa_exception_fp_ieee_overflow 0
		.amdhsa_exception_fp_ieee_underflow 0
		.amdhsa_exception_fp_ieee_inexact 0
		.amdhsa_exception_int_div_zero 0
	.end_amdhsa_kernel

amdhsa.kernels:
  - .agpr_count:     0
    .args:
      - .actual_access:  read_only
        .address_space:  global
        .offset:         0
        .size:           8
        .value_kind:     global_buffer
      - .actual_access:  read_only
        .address_space:  global
        .offset:         8
        .size:           8
        .value_kind:     global_buffer
      - .actual_access:  read_only
        .address_space:  global
        .offset:         16
        .size:           8
        .value_kind:     global_buffer
      - .actual_access:  read_only
        .address_space:  global
        .offset:         24
        .size:           8
        .value_kind:     global_buffer
      - .actual_access:  read_only
        .address_space:  global
        .offset:         32
        .size:           8
        .value_kind:     global_buffer
      - .address_space:  global
        .offset:         40
        .size:           8
        .value_kind:     global_buffer
      - .actual_access:  write_only
        .address_space:  global
        .offset:         48
        .size:           8
        .value_kind:     global_buffer
      - .actual_access:  write_only
        .address_space:  global
        .offset:         56
        .size:           8
        .value_kind:     global_buffer
      - .actual_access:  write_only
        .address_space:  global
        .offset:         64
        .size:           8
        .value_kind:     global_buffer
    .group_segment_fixed_size: 21520
    .kernarg_segment_align: 8
    .kernarg_segment_size: 72
    .language:       OpenCL C
    .language_version:
      - 2
      - 0
    .max_flat_workgroup_size: 256
    .name:           _Z11prep_kernelPKfS0_S0_S0_S0_PtS1_PfS1_
    .private_segment_fixed_size: 0
    .sgpr_count:     20
    .sgpr_spill_count: 0
    .symbol:         _Z11prep_kernelPKfS0_S0_S0_S0_PtS1_PfS1_.kd
    .uniform_work_group_size: 1
    .uses_dynamic_stack: false
    .vgpr_count:     70
    .vgpr_spill_count: 0
    .wavefront_size: 64
  - .agpr_count:     0
    .args:
      - .address_space:  global
        .offset:         0
        .size:           8
        .value_kind:     global_buffer
      - .address_space:  global
        .offset:         8
        .size:           8
        .value_kind:     global_buffer
      - .actual_access:  read_only
        .address_space:  global
        .offset:         16
        .size:           8
        .value_kind:     global_buffer
      - .address_space:  global
        .offset:         24
        .size:           8
        .value_kind:     global_buffer
      - .actual_access:  read_only
        .address_space:  global
        .offset:         32
        .size:           8
        .value_kind:     global_buffer
      - .actual_access:  read_only
        .address_space:  global
        .offset:         40
        .size:           8
        .value_kind:     global_buffer
      - .actual_access:  write_only
        .address_space:  global
        .offset:         48
        .size:           8
        .value_kind:     global_buffer
    .group_segment_fixed_size: 0
    .kernarg_segment_align: 8
    .kernarg_segment_size: 56
    .language:       OpenCL C
    .language_version:
      - 2
      - 0
    .max_flat_workgroup_size: 512
    .name:           _Z12fused_kernelPKtS0_PKfS0_S2_S2_Pf
    .private_segment_fixed_size: 0
    .sgpr_count:     54
    .sgpr_spill_count: 0
    .symbol:         _Z12fused_kernelPKtS0_PKfS0_S2_S2_Pf.kd
    .uniform_work_group_size: 1
    .uses_dynamic_stack: false
    .vgpr_count:     246
    .vgpr_spill_count: 0
    .wavefront_size: 64
